# v059
# speedup vs baseline: 1.1398x; 1.0097x over previous
.Lmy_epi_last:
	s_cmp_eq_u32 s30, 7
	s_cbranch_scc1 .Lmy_epi_l7
	v_exp_f32_e32 v120, v120
	v_exp_f32_e32 v121, v121
	v_exp_f32_e32 v122, v122
	v_pk_add_f32 v[120:121], v[120:121], 1.0 op_sel_hi:[1,0]
	v_exp_f32_e32 v123, v123
	v_exp_f32_e32 v124, v124
	v_pk_add_f32 v[122:123], v[122:123], 1.0 op_sel_hi:[1,0]
	v_exp_f32_e32 v125, v125
	v_exp_f32_e32 v126, v126
	v_pk_add_f32 v[124:125], v[124:125], 1.0 op_sel_hi:[1,0]
	v_exp_f32_e32 v127, v127
	v_exp_f32_e32 v116, v116
	v_pk_add_f32 v[126:127], v[126:127], 1.0 op_sel_hi:[1,0]
	v_exp_f32_e32 v117, v117
	v_pk_mul_f32 v[120:121], v[120:121], v[124:125]
	v_exp_f32_e32 v118, v118
	v_pk_mul_f32 v[122:123], v[122:123], v[126:127]
	v_exp_f32_e32 v119, v119
	v_pk_add_f32 v[124:125], v[124:125], 2.0 op_sel_hi:[1,0] neg_lo:[1,0] neg_hi:[1,0]
	v_pk_add_f32 v[116:117], v[116:117], 1.0 op_sel_hi:[1,0]
	v_pk_add_f32 v[126:127], v[126:127], 2.0 op_sel_hi:[1,0] neg_lo:[1,0] neg_hi:[1,0]
	v_pk_add_f32 v[118:119], v[118:119], 1.0 op_sel_hi:[1,0]
	v_pk_mul_f32 v[124:125], v[124:125], v[116:117]
	v_pk_mul_f32 v[116:117], v[116:117], v[120:121]
	v_pk_mul_f32 v[126:127], v[126:127], v[118:119]
	v_pk_mul_f32 v[118:119], v[118:119], v[122:123]
	v_rcp_f32_e32 v116, v116
	v_rcp_f32_e32 v117, v117
	v_rcp_f32_e32 v118, v118
	v_rcp_f32_e32 v119, v119
	s_waitcnt lgkmcnt(3)
	v_pk_fma_f32 v[124:125], v[172:173], v[120:121], v[124:125]
	v_pk_fma_f32 v[126:127], v[174:175], v[122:123], v[126:127]
	v_pk_mul_f32 v[116:117], v[116:117], v[124:125]
	v_pk_mul_f32 v[118:119], v[118:119], v[126:127]
	global_store_dwordx4 v[176:177], v[116:119], off sc1
	s_nop 1
	v_pk_mul_f32 v[116:117], v[116:117], s[96:97] op_sel_hi:[1,0]
	v_pk_mul_f32 v[118:119], v[118:119], s[96:97] op_sel_hi:[1,0]
	v_exp_f32_e32 v112, v112
	v_exp_f32_e32 v113, v113
	v_exp_f32_e32 v114, v114
	v_pk_fma_f32 v[112:113], v[112:113], s[98:99], s[98:99] op_sel_hi:[1,0,0]
	v_exp_f32_e32 v115, v115
	v_exp_f32_e32 v116, v116
	v_pk_fma_f32 v[114:115], v[114:115], s[98:99], s[98:99] op_sel_hi:[1,0,0]
	v_exp_f32_e32 v117, v117
	v_exp_f32_e32 v118, v118
	v_pk_add_f32 v[116:117], v[116:117], 1.0 op_sel_hi:[1,0]
	v_exp_f32_e32 v119, v119
	v_pk_mul_f32 v[112:113], v[112:113], v[116:117]
	v_rcp_f32_e32 v112, v112
	v_pk_add_f32 v[118:119], v[118:119], 1.0 op_sel_hi:[1,0]
	v_rcp_f32_e32 v113, v113
	v_pk_mul_f32 v[114:115], v[114:115], v[118:119]
	v_pk_add_f32 v[116:117], v[116:117], 2.0 op_sel_hi:[1,0] neg_lo:[1,0] neg_hi:[1,0]
	v_rcp_f32_e32 v114, v114
	v_rcp_f32_e32 v115, v115
	v_pk_add_f32 v[118:119], v[118:119], 2.0 op_sel_hi:[1,0] neg_lo:[1,0] neg_hi:[1,0]
	v_pk_mul_f32 v[112:113], v[112:113], v[116:117]
	v_pk_mul_f32 v[114:115], v[114:115], v[118:119]
	v_cvt_pk_fp8_f32 v124, v112, v113
	s_add_u32 s0, s8, s27
	s_addc_u32 s1, s9, 0
	s_ashr_i32 s35, s34, 31
	s_lshl_b64 s[34:35], s[34:35], 21
	v_ashrrev_i32_e32 v209, 31, v208
	s_add_u32 s36, s73, s34
	v_lshrrev_b32_e32 v126, 4, v210
	v_and_b32_e32 v127, 15, v210
	v_lshl_or_b32 v126, v126, 8, v127
	v_and_b32_e32 v127, 15, v208
	v_mul_u32_u24_e32 v127, 0x3f0, v127
	v_sub_u32_e32 v126, v126, v127
	v_ashrrev_i32_e32 v127, 31, v126
	v_lshl_add_u64 v[122:123], s[0:1], 0, v[126:127]
	v_cvt_pk_fp8_f32 v124, v114, v115 op_sel:[0,0,1]
	v_lshlrev_b64 v[116:117], 10, v[208:209]
	s_addc_u32 s37, s74, s35
	v_lshl_add_u64 v[118:119], v[122:123], 0, v[116:117]
	global_store_dword v[118:119], v124, off sc1
	s_cmp_eq_u32 s30, 7
	s_cselect_b64 s[34:35], -1, 0
	s_cmp_lg_u32 s30, 7
	v_lshrrev_b32_e32 v126, 4, v210
	v_lshlrev_b32_e32 v126, 9, v126
	v_and_b32_e32 v127, 15, v210
	v_lshl_or_b32 v126, v127, 1, v126
	v_and_b32_e32 v127, 15, v208
	v_mul_u32_u24_e32 v127, 0x7e0, v127
	v_sub_u32_e32 v126, v126, v127
	v_ashrrev_i32_e32 v127, 31, v126
	v_lshl_add_u64 v[120:121], s[36:37], 0, v[126:127]
	v_exp_f32_e32 v104, v104
	v_exp_f32_e32 v105, v105
	v_exp_f32_e32 v106, v106
	v_pk_add_f32 v[104:105], v[104:105], 1.0 op_sel_hi:[1,0]
	v_exp_f32_e32 v107, v107
	v_exp_f32_e32 v108, v108
	v_pk_add_f32 v[106:107], v[106:107], 1.0 op_sel_hi:[1,0]
	v_exp_f32_e32 v109, v109
	v_exp_f32_e32 v110, v110
	v_pk_add_f32 v[108:109], v[108:109], 1.0 op_sel_hi:[1,0]
	v_exp_f32_e32 v111, v111
	v_exp_f32_e32 v100, v100
	v_pk_add_f32 v[110:111], v[110:111], 1.0 op_sel_hi:[1,0]
	v_exp_f32_e32 v101, v101
	v_pk_mul_f32 v[104:105], v[104:105], v[108:109]
	v_exp_f32_e32 v102, v102
	v_pk_mul_f32 v[106:107], v[106:107], v[110:111]
	v_exp_f32_e32 v103, v103
	v_pk_add_f32 v[108:109], v[108:109], 2.0 op_sel_hi:[1,0] neg_lo:[1,0] neg_hi:[1,0]
	v_pk_add_f32 v[100:101], v[100:101], 1.0 op_sel_hi:[1,0]
	v_pk_add_f32 v[110:111], v[110:111], 2.0 op_sel_hi:[1,0] neg_lo:[1,0] neg_hi:[1,0]
	v_pk_add_f32 v[102:103], v[102:103], 1.0 op_sel_hi:[1,0]
	v_pk_mul_f32 v[108:109], v[108:109], v[100:101]
	v_pk_mul_f32 v[100:101], v[100:101], v[104:105]
	v_pk_mul_f32 v[110:111], v[110:111], v[102:103]
	v_pk_mul_f32 v[102:103], v[102:103], v[106:107]
	v_rcp_f32_e32 v100, v100
	v_rcp_f32_e32 v101, v101
	v_rcp_f32_e32 v102, v102
	v_rcp_f32_e32 v103, v103
	s_waitcnt lgkmcnt(2)
	v_pk_fma_f32 v[108:109], v[168:169], v[104:105], v[108:109]
	v_pk_fma_f32 v[110:111], v[170:171], v[106:107], v[110:111]
	v_lshl_add_u64 v[104:105], v[176:177], 0, s[18:19]
	v_pk_mul_f32 v[100:101], v[100:101], v[108:109]
	v_pk_mul_f32 v[102:103], v[102:103], v[110:111]
	global_store_dwordx4 v[104:105], v[100:103], off sc1
	s_nop 1
	v_pk_mul_f32 v[100:101], v[100:101], s[96:97] op_sel_hi:[1,0]
	v_pk_mul_f32 v[102:103], v[102:103], s[96:97] op_sel_hi:[1,0]
	v_exp_f32_e32 v96, v96
	v_exp_f32_e32 v97, v97
	v_exp_f32_e32 v98, v98
	v_pk_fma_f32 v[96:97], v[96:97], s[98:99], s[98:99] op_sel_hi:[1,0,0]
	v_exp_f32_e32 v99, v99
	v_exp_f32_e32 v100, v100
	v_pk_fma_f32 v[98:99], v[98:99], s[98:99], s[98:99] op_sel_hi:[1,0,0]
	v_exp_f32_e32 v101, v101
	v_exp_f32_e32 v102, v102
	v_pk_add_f32 v[100:101], v[100:101], 1.0 op_sel_hi:[1,0]
	v_exp_f32_e32 v103, v103
	v_pk_mul_f32 v[96:97], v[96:97], v[100:101]
	v_rcp_f32_e32 v96, v96
	v_pk_add_f32 v[102:103], v[102:103], 1.0 op_sel_hi:[1,0]
	v_rcp_f32_e32 v97, v97
	v_pk_mul_f32 v[98:99], v[98:99], v[102:103]
	v_pk_add_f32 v[100:101], v[100:101], 2.0 op_sel_hi:[1,0] neg_lo:[1,0] neg_hi:[1,0]
	v_rcp_f32_e32 v98, v98
	v_rcp_f32_e32 v99, v99
	v_pk_add_f32 v[102:103], v[102:103], 2.0 op_sel_hi:[1,0] neg_lo:[1,0] neg_hi:[1,0]
	v_pk_mul_f32 v[96:97], v[96:97], v[100:101]
	v_pk_mul_f32 v[98:99], v[98:99], v[102:103]
	v_cvt_pk_fp8_f32 v104, v96, v97
	v_ashrrev_i32_e32 v207, 31, v206
	v_lshlrev_b64 v[100:101], 10, v[206:207]
	v_lshl_add_u64 v[102:103], v[122:123], 0, v[100:101]
	v_cvt_pk_fp8_f32 v104, v98, v99 op_sel:[0,0,1]
	v_cndmask_b32_e64 v105, 0, 1, s[34:35]
	global_store_dword v[102:103], v104, off sc1
	v_cmp_ne_u32_e64 s[0:1], 1, v105
	v_exp_f32_e32 v88, v88
	v_exp_f32_e32 v89, v89
	v_exp_f32_e32 v90, v90
	v_pk_add_f32 v[88:89], v[88:89], 1.0 op_sel_hi:[1,0]
	v_exp_f32_e32 v91, v91
	v_exp_f32_e32 v92, v92
	v_pk_add_f32 v[90:91], v[90:91], 1.0 op_sel_hi:[1,0]
	v_exp_f32_e32 v93, v93
	v_exp_f32_e32 v94, v94
	v_pk_add_f32 v[92:93], v[92:93], 1.0 op_sel_hi:[1,0]
	v_exp_f32_e32 v95, v95
	v_exp_f32_e32 v84, v84
	v_pk_add_f32 v[94:95], v[94:95], 1.0 op_sel_hi:[1,0]
	v_exp_f32_e32 v85, v85
	v_pk_mul_f32 v[88:89], v[88:89], v[92:93]
	v_exp_f32_e32 v86, v86
	v_pk_mul_f32 v[90:91], v[90:91], v[94:95]
	v_exp_f32_e32 v87, v87
	v_pk_add_f32 v[92:93], v[92:93], 2.0 op_sel_hi:[1,0] neg_lo:[1,0] neg_hi:[1,0]
	v_pk_add_f32 v[84:85], v[84:85], 1.0 op_sel_hi:[1,0]
	v_pk_add_f32 v[94:95], v[94:95], 2.0 op_sel_hi:[1,0] neg_lo:[1,0] neg_hi:[1,0]
	v_pk_add_f32 v[86:87], v[86:87], 1.0 op_sel_hi:[1,0]
	v_pk_mul_f32 v[92:93], v[92:93], v[84:85]
	v_pk_mul_f32 v[84:85], v[84:85], v[88:89]
	v_pk_mul_f32 v[94:95], v[94:95], v[86:87]
	v_pk_mul_f32 v[86:87], v[86:87], v[90:91]
	v_rcp_f32_e32 v84, v84
	v_rcp_f32_e32 v85, v85
	v_rcp_f32_e32 v86, v86
	v_rcp_f32_e32 v87, v87
	s_waitcnt lgkmcnt(1)
	v_pk_fma_f32 v[92:93], v[164:165], v[88:89], v[92:93]
	v_pk_fma_f32 v[94:95], v[166:167], v[90:91], v[94:95]
	v_pk_mul_f32 v[84:85], v[84:85], v[92:93]
	v_pk_mul_f32 v[86:87], v[86:87], v[94:95]
	v_lshl_add_u64 v[88:89], v[176:177], 0, s[12:13]
	global_store_dwordx4 v[88:89], v[84:87], off sc1
	s_nop 1
	v_pk_mul_f32 v[84:85], v[84:85], s[96:97] op_sel_hi:[1,0]
	v_pk_mul_f32 v[86:87], v[86:87], s[96:97] op_sel_hi:[1,0]
	v_exp_f32_e32 v80, v80
	v_exp_f32_e32 v81, v81
	v_exp_f32_e32 v82, v82
	v_pk_fma_f32 v[80:81], v[80:81], s[98:99], s[98:99] op_sel_hi:[1,0,0]
	v_exp_f32_e32 v83, v83
	v_exp_f32_e32 v84, v84
	v_pk_fma_f32 v[82:83], v[82:83], s[98:99], s[98:99] op_sel_hi:[1,0,0]
	v_exp_f32_e32 v85, v85
	v_exp_f32_e32 v86, v86
	v_pk_add_f32 v[84:85], v[84:85], 1.0 op_sel_hi:[1,0]
	v_exp_f32_e32 v87, v87
	v_pk_mul_f32 v[80:81], v[80:81], v[84:85]
	v_rcp_f32_e32 v80, v80
	v_pk_add_f32 v[86:87], v[86:87], 1.0 op_sel_hi:[1,0]
	v_rcp_f32_e32 v81, v81
	v_pk_mul_f32 v[82:83], v[82:83], v[86:87]
	v_pk_add_f32 v[84:85], v[84:85], 2.0 op_sel_hi:[1,0] neg_lo:[1,0] neg_hi:[1,0]
	v_rcp_f32_e32 v82, v82
	v_rcp_f32_e32 v83, v83
	v_pk_add_f32 v[86:87], v[86:87], 2.0 op_sel_hi:[1,0] neg_lo:[1,0] neg_hi:[1,0]
	v_pk_mul_f32 v[80:81], v[80:81], v[84:85]
	v_pk_mul_f32 v[82:83], v[82:83], v[86:87]
	v_ashrrev_i32_e32 v205, 31, v204
	v_cvt_pk_fp8_f32 v88, v80, v81
	s_and_b64 vcc, exec, s[0:1]
	v_cvt_pk_fp8_f32 v88, v82, v83 op_sel:[0,0,1]
	v_lshlrev_b64 v[84:85], 10, v[204:205]
	v_lshl_add_u64 v[86:87], v[122:123], 0, v[84:85]
	global_store_dword v[86:87], v88, off sc1
	v_exp_f32_e32 v72, v72
	v_exp_f32_e32 v73, v73
	v_exp_f32_e32 v74, v74
	v_pk_add_f32 v[72:73], v[72:73], 1.0 op_sel_hi:[1,0]
	v_exp_f32_e32 v75, v75
	v_exp_f32_e32 v76, v76
	v_pk_add_f32 v[74:75], v[74:75], 1.0 op_sel_hi:[1,0]
	v_exp_f32_e32 v77, v77
	v_exp_f32_e32 v78, v78
	v_pk_add_f32 v[76:77], v[76:77], 1.0 op_sel_hi:[1,0]
	v_exp_f32_e32 v79, v79
	v_exp_f32_e32 v68, v68
	v_pk_add_f32 v[78:79], v[78:79], 1.0 op_sel_hi:[1,0]
	v_exp_f32_e32 v69, v69
	v_pk_mul_f32 v[72:73], v[72:73], v[76:77]
	v_exp_f32_e32 v70, v70
	v_pk_mul_f32 v[74:75], v[74:75], v[78:79]
	v_exp_f32_e32 v71, v71
	v_pk_add_f32 v[76:77], v[76:77], 2.0 op_sel_hi:[1,0] neg_lo:[1,0] neg_hi:[1,0]
	v_pk_add_f32 v[68:69], v[68:69], 1.0 op_sel_hi:[1,0]
	v_pk_add_f32 v[78:79], v[78:79], 2.0 op_sel_hi:[1,0] neg_lo:[1,0] neg_hi:[1,0]
	v_pk_add_f32 v[70:71], v[70:71], 1.0 op_sel_hi:[1,0]
	v_pk_mul_f32 v[76:77], v[76:77], v[68:69]
	v_pk_mul_f32 v[68:69], v[68:69], v[72:73]
	v_pk_mul_f32 v[78:79], v[78:79], v[70:71]
	v_pk_mul_f32 v[70:71], v[70:71], v[74:75]
	v_rcp_f32_e32 v68, v68
	v_rcp_f32_e32 v69, v69
	v_rcp_f32_e32 v70, v70
	v_rcp_f32_e32 v71, v71
	s_waitcnt lgkmcnt(0)
	v_pk_fma_f32 v[76:77], v[160:161], v[72:73], v[76:77]
	v_pk_fma_f32 v[78:79], v[162:163], v[74:75], v[78:79]
	v_lshl_add_u64 v[72:73], v[176:177], 0, s[20:21]
	v_pk_mul_f32 v[68:69], v[68:69], v[76:77]
	v_pk_mul_f32 v[70:71], v[70:71], v[78:79]
	global_store_dwordx4 v[72:73], v[68:71], off sc1
	s_nop 1
	v_pk_mul_f32 v[68:69], v[68:69], s[96:97] op_sel_hi:[1,0]
	v_pk_mul_f32 v[70:71], v[70:71], s[96:97] op_sel_hi:[1,0]
	v_exp_f32_e32 v64, v64
	v_exp_f32_e32 v65, v65
	v_exp_f32_e32 v66, v66
	v_pk_fma_f32 v[64:65], v[64:65], s[98:99], s[98:99] op_sel_hi:[1,0,0]
	v_exp_f32_e32 v67, v67
	v_exp_f32_e32 v68, v68
	v_pk_fma_f32 v[66:67], v[66:67], s[98:99], s[98:99] op_sel_hi:[1,0,0]
	v_exp_f32_e32 v69, v69
	v_exp_f32_e32 v70, v70
	v_pk_add_f32 v[68:69], v[68:69], 1.0 op_sel_hi:[1,0]
	v_exp_f32_e32 v71, v71
	v_pk_mul_f32 v[64:65], v[64:65], v[68:69]
	v_rcp_f32_e32 v64, v64
	v_pk_add_f32 v[70:71], v[70:71], 1.0 op_sel_hi:[1,0]
	v_rcp_f32_e32 v65, v65
	v_pk_mul_f32 v[66:67], v[66:67], v[70:71]
	v_pk_add_f32 v[68:69], v[68:69], 2.0 op_sel_hi:[1,0] neg_lo:[1,0] neg_hi:[1,0]
	v_rcp_f32_e32 v66, v66
	v_rcp_f32_e32 v67, v67
	v_pk_add_f32 v[70:71], v[70:71], 2.0 op_sel_hi:[1,0] neg_lo:[1,0] neg_hi:[1,0]
	v_pk_mul_f32 v[64:65], v[64:65], v[68:69]
	v_pk_mul_f32 v[66:67], v[66:67], v[70:71]
	v_ashrrev_i32_e32 v203, 31, v202
	v_cvt_pk_fp8_f32 v72, v64, v65
	s_and_b64 vcc, exec, s[0:1]
	v_cvt_pk_fp8_f32 v72, v66, v67 op_sel:[0,0,1]
	v_lshlrev_b64 v[68:69], 10, v[202:203]
	v_lshl_add_u64 v[70:71], v[122:123], 0, v[68:69]
	global_store_dword v[70:71], v72, off sc1
	v_exp_f32_e32 v56, v56
	v_exp_f32_e32 v57, v57
	v_exp_f32_e32 v58, v58
	v_pk_add_f32 v[56:57], v[56:57], 1.0 op_sel_hi:[1,0]
	v_exp_f32_e32 v59, v59
	v_exp_f32_e32 v60, v60
	v_pk_add_f32 v[58:59], v[58:59], 1.0 op_sel_hi:[1,0]
	v_exp_f32_e32 v61, v61
	v_exp_f32_e32 v62, v62
	v_pk_add_f32 v[60:61], v[60:61], 1.0 op_sel_hi:[1,0]
	v_exp_f32_e32 v63, v63
	v_exp_f32_e32 v52, v52
	v_pk_add_f32 v[62:63], v[62:63], 1.0 op_sel_hi:[1,0]
	v_exp_f32_e32 v53, v53
	v_pk_mul_f32 v[56:57], v[56:57], v[60:61]
	v_exp_f32_e32 v54, v54
	v_pk_mul_f32 v[58:59], v[58:59], v[62:63]
	v_exp_f32_e32 v55, v55
	v_pk_add_f32 v[60:61], v[60:61], 2.0 op_sel_hi:[1,0] neg_lo:[1,0] neg_hi:[1,0]
	v_pk_add_f32 v[52:53], v[52:53], 1.0 op_sel_hi:[1,0]
	v_pk_add_f32 v[62:63], v[62:63], 2.0 op_sel_hi:[1,0] neg_lo:[1,0] neg_hi:[1,0]
	v_pk_add_f32 v[54:55], v[54:55], 1.0 op_sel_hi:[1,0]
	v_pk_mul_f32 v[60:61], v[60:61], v[52:53]
	v_pk_mul_f32 v[52:53], v[52:53], v[56:57]
	v_pk_mul_f32 v[62:63], v[62:63], v[54:55]
	v_pk_mul_f32 v[54:55], v[54:55], v[58:59]
	v_rcp_f32_e32 v52, v52
	v_rcp_f32_e32 v53, v53
	v_rcp_f32_e32 v54, v54
	v_rcp_f32_e32 v55, v55
	s_waitcnt vmcnt(8)
	v_pk_fma_f32 v[60:61], v[156:157], v[56:57], v[60:61]
	v_pk_fma_f32 v[62:63], v[158:159], v[58:59], v[62:63]
	v_pk_mul_f32 v[52:53], v[52:53], v[60:61]
	v_pk_mul_f32 v[54:55], v[54:55], v[62:63]
	v_lshl_add_u64 v[56:57], v[176:177], 0, s[14:15]
	global_store_dwordx4 v[56:57], v[52:55], off sc1
	s_nop 1
	v_pk_mul_f32 v[52:53], v[52:53], s[96:97] op_sel_hi:[1,0]
	v_pk_mul_f32 v[54:55], v[54:55], s[96:97] op_sel_hi:[1,0]
	v_exp_f32_e32 v48, v48
	v_exp_f32_e32 v49, v49
	v_exp_f32_e32 v50, v50
	v_pk_fma_f32 v[48:49], v[48:49], s[98:99], s[98:99] op_sel_hi:[1,0,0]
	v_exp_f32_e32 v51, v51
	v_exp_f32_e32 v52, v52
	v_pk_fma_f32 v[50:51], v[50:51], s[98:99], s[98:99] op_sel_hi:[1,0,0]
	v_exp_f32_e32 v53, v53
	v_exp_f32_e32 v54, v54
	v_pk_add_f32 v[52:53], v[52:53], 1.0 op_sel_hi:[1,0]
	v_exp_f32_e32 v55, v55
	v_pk_mul_f32 v[48:49], v[48:49], v[52:53]
	v_rcp_f32_e32 v48, v48
	v_pk_add_f32 v[54:55], v[54:55], 1.0 op_sel_hi:[1,0]
	v_rcp_f32_e32 v49, v49
	v_pk_mul_f32 v[50:51], v[50:51], v[54:55]
	v_pk_add_f32 v[52:53], v[52:53], 2.0 op_sel_hi:[1,0] neg_lo:[1,0] neg_hi:[1,0]
	v_rcp_f32_e32 v50, v50
	v_rcp_f32_e32 v51, v51
	v_pk_add_f32 v[54:55], v[54:55], 2.0 op_sel_hi:[1,0] neg_lo:[1,0] neg_hi:[1,0]
	v_pk_mul_f32 v[48:49], v[48:49], v[52:53]
	v_pk_mul_f32 v[50:51], v[50:51], v[54:55]
	v_ashrrev_i32_e32 v201, 31, v200
	v_cvt_pk_fp8_f32 v56, v48, v49
	s_and_b64 vcc, exec, s[0:1]
	v_cvt_pk_fp8_f32 v56, v50, v51 op_sel:[0,0,1]
	v_lshlrev_b64 v[52:53], 10, v[200:201]
	v_lshl_add_u64 v[54:55], v[122:123], 0, v[52:53]
	global_store_dword v[54:55], v56, off sc1
	v_exp_f32_e32 v40, v40
	v_exp_f32_e32 v41, v41
	v_exp_f32_e32 v42, v42
	v_pk_add_f32 v[40:41], v[40:41], 1.0 op_sel_hi:[1,0]
	v_exp_f32_e32 v43, v43
	v_exp_f32_e32 v44, v44
	v_pk_add_f32 v[42:43], v[42:43], 1.0 op_sel_hi:[1,0]
	v_exp_f32_e32 v45, v45
	v_exp_f32_e32 v46, v46
	v_pk_add_f32 v[44:45], v[44:45], 1.0 op_sel_hi:[1,0]
	v_exp_f32_e32 v47, v47
	v_exp_f32_e32 v36, v36
	v_pk_add_f32 v[46:47], v[46:47], 1.0 op_sel_hi:[1,0]
	v_exp_f32_e32 v37, v37
	v_pk_mul_f32 v[40:41], v[40:41], v[44:45]
	v_exp_f32_e32 v38, v38
	v_pk_mul_f32 v[42:43], v[42:43], v[46:47]
	v_exp_f32_e32 v39, v39
	v_pk_add_f32 v[44:45], v[44:45], 2.0 op_sel_hi:[1,0] neg_lo:[1,0] neg_hi:[1,0]
	v_pk_add_f32 v[36:37], v[36:37], 1.0 op_sel_hi:[1,0]
	v_pk_add_f32 v[46:47], v[46:47], 2.0 op_sel_hi:[1,0] neg_lo:[1,0] neg_hi:[1,0]
	v_pk_add_f32 v[38:39], v[38:39], 1.0 op_sel_hi:[1,0]
	v_pk_mul_f32 v[44:45], v[44:45], v[36:37]
	v_pk_mul_f32 v[36:37], v[36:37], v[40:41]
	v_pk_mul_f32 v[46:47], v[46:47], v[38:39]
	v_pk_mul_f32 v[38:39], v[38:39], v[42:43]
	v_rcp_f32_e32 v36, v36
	v_rcp_f32_e32 v37, v37
	v_rcp_f32_e32 v38, v38
	v_rcp_f32_e32 v39, v39
	v_pk_fma_f32 v[44:45], v[152:153], v[40:41], v[44:45]
	v_pk_fma_f32 v[46:47], v[154:155], v[42:43], v[46:47]
	v_lshl_add_u64 v[40:41], v[176:177], 0, s[22:23]
	v_pk_mul_f32 v[36:37], v[36:37], v[44:45]
	v_pk_mul_f32 v[38:39], v[38:39], v[46:47]
	global_store_dwordx4 v[40:41], v[36:39], off sc1
	s_nop 1
	v_pk_mul_f32 v[36:37], v[36:37], s[96:97] op_sel_hi:[1,0]
	v_pk_mul_f32 v[38:39], v[38:39], s[96:97] op_sel_hi:[1,0]
	v_exp_f32_e32 v32, v32
	v_exp_f32_e32 v33, v33
	v_exp_f32_e32 v34, v34
	v_pk_fma_f32 v[32:33], v[32:33], s[98:99], s[98:99] op_sel_hi:[1,0,0]
	v_exp_f32_e32 v35, v35
	v_exp_f32_e32 v36, v36
	v_pk_fma_f32 v[34:35], v[34:35], s[98:99], s[98:99] op_sel_hi:[1,0,0]
	v_exp_f32_e32 v37, v37
	v_exp_f32_e32 v38, v38
	v_pk_add_f32 v[36:37], v[36:37], 1.0 op_sel_hi:[1,0]
	v_exp_f32_e32 v39, v39
	v_pk_mul_f32 v[32:33], v[32:33], v[36:37]
	v_rcp_f32_e32 v32, v32
	v_pk_add_f32 v[38:39], v[38:39], 1.0 op_sel_hi:[1,0]
	v_rcp_f32_e32 v33, v33
	v_pk_mul_f32 v[34:35], v[34:35], v[38:39]
	v_pk_add_f32 v[36:37], v[36:37], 2.0 op_sel_hi:[1,0] neg_lo:[1,0] neg_hi:[1,0]
	v_rcp_f32_e32 v34, v34
	v_rcp_f32_e32 v35, v35
	v_pk_add_f32 v[38:39], v[38:39], 2.0 op_sel_hi:[1,0] neg_lo:[1,0] neg_hi:[1,0]
	v_pk_mul_f32 v[32:33], v[32:33], v[36:37]
	v_pk_mul_f32 v[34:35], v[34:35], v[38:39]
	v_cvt_pk_fp8_f32 v40, v32, v33
	v_or_b32_e32 v36, 16, v200
	v_ashrrev_i32_e32 v37, 31, v36
	v_lshlrev_b64 v[36:37], 10, v[36:37]
	v_cvt_pk_fp8_f32 v40, v34, v35 op_sel:[0,0,1]
	v_lshl_add_u64 v[38:39], v[122:123], 0, v[36:37]
	global_store_dword v[38:39], v40, off sc1
	v_exp_f32_e32 v24, v24
	v_exp_f32_e32 v25, v25
	v_exp_f32_e32 v26, v26
	v_pk_add_f32 v[24:25], v[24:25], 1.0 op_sel_hi:[1,0]
	v_exp_f32_e32 v27, v27
	v_exp_f32_e32 v28, v28
	v_pk_add_f32 v[26:27], v[26:27], 1.0 op_sel_hi:[1,0]
	v_exp_f32_e32 v29, v29
	v_exp_f32_e32 v30, v30
	v_pk_add_f32 v[28:29], v[28:29], 1.0 op_sel_hi:[1,0]
	v_exp_f32_e32 v31, v31
	v_exp_f32_e32 v20, v20
	v_pk_add_f32 v[30:31], v[30:31], 1.0 op_sel_hi:[1,0]
	v_exp_f32_e32 v21, v21
	v_pk_mul_f32 v[24:25], v[24:25], v[28:29]
	v_exp_f32_e32 v22, v22
	v_pk_mul_f32 v[26:27], v[26:27], v[30:31]
	v_exp_f32_e32 v23, v23
	v_pk_add_f32 v[28:29], v[28:29], 2.0 op_sel_hi:[1,0] neg_lo:[1,0] neg_hi:[1,0]
	v_pk_add_f32 v[20:21], v[20:21], 1.0 op_sel_hi:[1,0]
	v_pk_add_f32 v[30:31], v[30:31], 2.0 op_sel_hi:[1,0] neg_lo:[1,0] neg_hi:[1,0]
	v_pk_add_f32 v[22:23], v[22:23], 1.0 op_sel_hi:[1,0]
	v_pk_mul_f32 v[28:29], v[28:29], v[20:21]
	v_pk_mul_f32 v[20:21], v[20:21], v[24:25]
	v_pk_mul_f32 v[30:31], v[30:31], v[22:23]
	v_pk_mul_f32 v[22:23], v[22:23], v[26:27]
	v_rcp_f32_e32 v20, v20
	v_rcp_f32_e32 v21, v21
	v_rcp_f32_e32 v22, v22
	v_rcp_f32_e32 v23, v23
	v_pk_fma_f32 v[28:29], v[148:149], v[24:25], v[28:29]
	v_pk_fma_f32 v[30:31], v[150:151], v[26:27], v[30:31]
	v_pk_mul_f32 v[20:21], v[20:21], v[28:29]
	v_pk_mul_f32 v[22:23], v[22:23], v[30:31]
	v_lshl_add_u64 v[24:25], v[176:177], 0, s[16:17]
	global_store_dwordx4 v[24:25], v[20:23], off sc1
	s_nop 1
	v_pk_mul_f32 v[20:21], v[20:21], s[96:97] op_sel_hi:[1,0]
	v_pk_mul_f32 v[22:23], v[22:23], s[96:97] op_sel_hi:[1,0]
	v_exp_f32_e32 v16, v16
	v_exp_f32_e32 v17, v17
	v_exp_f32_e32 v18, v18
	v_pk_fma_f32 v[16:17], v[16:17], s[98:99], s[98:99] op_sel_hi:[1,0,0]
	v_exp_f32_e32 v19, v19
	v_exp_f32_e32 v20, v20
	v_pk_fma_f32 v[18:19], v[18:19], s[98:99], s[98:99] op_sel_hi:[1,0,0]
	v_exp_f32_e32 v21, v21
	v_exp_f32_e32 v22, v22
	v_pk_add_f32 v[20:21], v[20:21], 1.0 op_sel_hi:[1,0]
	v_exp_f32_e32 v23, v23
	v_pk_mul_f32 v[16:17], v[16:17], v[20:21]
	v_rcp_f32_e32 v16, v16
	v_pk_add_f32 v[22:23], v[22:23], 1.0 op_sel_hi:[1,0]
	v_rcp_f32_e32 v17, v17
	v_pk_mul_f32 v[18:19], v[18:19], v[22:23]
	v_pk_add_f32 v[20:21], v[20:21], 2.0 op_sel_hi:[1,0] neg_lo:[1,0] neg_hi:[1,0]
	v_rcp_f32_e32 v18, v18
	v_rcp_f32_e32 v19, v19
	v_pk_add_f32 v[22:23], v[22:23], 2.0 op_sel_hi:[1,0] neg_lo:[1,0] neg_hi:[1,0]
	v_pk_mul_f32 v[16:17], v[16:17], v[20:21]
	v_pk_mul_f32 v[18:19], v[18:19], v[22:23]
	v_cvt_pk_fp8_f32 v24, v16, v17
	v_or_b32_e32 v20, 32, v200
	v_ashrrev_i32_e32 v21, 31, v20
	v_lshlrev_b64 v[20:21], 10, v[20:21]
	v_cvt_pk_fp8_f32 v24, v18, v19 op_sel:[0,0,1]
	v_lshl_add_u64 v[22:23], v[122:123], 0, v[20:21]
	global_store_dword v[22:23], v24, off sc1
	v_exp_f32_e32 v8, v8
	v_exp_f32_e32 v9, v9
	v_exp_f32_e32 v10, v10
	v_pk_add_f32 v[8:9], v[8:9], 1.0 op_sel_hi:[1,0]
	v_exp_f32_e32 v11, v11
	v_exp_f32_e32 v12, v12
	v_pk_add_f32 v[10:11], v[10:11], 1.0 op_sel_hi:[1,0]
	v_exp_f32_e32 v13, v13
	v_exp_f32_e32 v14, v14
	v_pk_add_f32 v[12:13], v[12:13], 1.0 op_sel_hi:[1,0]
	v_exp_f32_e32 v15, v15
	v_exp_f32_e32 v4, v4
	v_pk_add_f32 v[14:15], v[14:15], 1.0 op_sel_hi:[1,0]
	v_exp_f32_e32 v5, v5
	v_pk_mul_f32 v[8:9], v[8:9], v[12:13]
	v_exp_f32_e32 v6, v6
	v_pk_mul_f32 v[10:11], v[10:11], v[14:15]
	v_exp_f32_e32 v7, v7
	v_pk_add_f32 v[12:13], v[12:13], 2.0 op_sel_hi:[1,0] neg_lo:[1,0] neg_hi:[1,0]
	v_pk_add_f32 v[4:5], v[4:5], 1.0 op_sel_hi:[1,0]
	v_pk_add_f32 v[14:15], v[14:15], 2.0 op_sel_hi:[1,0] neg_lo:[1,0] neg_hi:[1,0]
	v_pk_add_f32 v[6:7], v[6:7], 1.0 op_sel_hi:[1,0]
	v_pk_mul_f32 v[12:13], v[12:13], v[4:5]
	v_pk_mul_f32 v[4:5], v[4:5], v[8:9]
	v_pk_mul_f32 v[14:15], v[14:15], v[6:7]
	v_pk_mul_f32 v[6:7], v[6:7], v[10:11]
	v_rcp_f32_e32 v4, v4
	v_rcp_f32_e32 v5, v5
	v_rcp_f32_e32 v6, v6
	v_rcp_f32_e32 v7, v7
	v_pk_fma_f32 v[12:13], v[144:145], v[8:9], v[12:13]
	v_pk_fma_f32 v[14:15], v[146:147], v[10:11], v[14:15]
	v_lshl_add_u64 v[8:9], v[176:177], 0, s[24:25]
	v_pk_mul_f32 v[4:5], v[4:5], v[12:13]
	v_pk_mul_f32 v[6:7], v[6:7], v[14:15]
	global_store_dwordx4 v[8:9], v[4:7], off sc1
	s_nop 1
	v_pk_mul_f32 v[4:5], v[4:5], s[96:97] op_sel_hi:[1,0]
	v_pk_mul_f32 v[6:7], v[6:7], s[96:97] op_sel_hi:[1,0]
	v_exp_f32_e32 v0, v0
	v_exp_f32_e32 v1, v1
	v_exp_f32_e32 v2, v2
	v_pk_fma_f32 v[0:1], v[0:1], s[98:99], s[98:99] op_sel_hi:[1,0,0]
	v_exp_f32_e32 v3, v3
	v_exp_f32_e32 v4, v4
	v_pk_fma_f32 v[2:3], v[2:3], s[98:99], s[98:99] op_sel_hi:[1,0,0]
	v_exp_f32_e32 v5, v5
	v_exp_f32_e32 v6, v6
	v_pk_add_f32 v[4:5], v[4:5], 1.0 op_sel_hi:[1,0]
	v_exp_f32_e32 v7, v7
	v_pk_mul_f32 v[0:1], v[0:1], v[4:5]
	v_rcp_f32_e32 v0, v0
	v_pk_add_f32 v[6:7], v[6:7], 1.0 op_sel_hi:[1,0]
	v_rcp_f32_e32 v1, v1
	v_pk_mul_f32 v[2:3], v[2:3], v[6:7]
	v_pk_add_f32 v[4:5], v[4:5], 2.0 op_sel_hi:[1,0] neg_lo:[1,0] neg_hi:[1,0]
	v_rcp_f32_e32 v2, v2
	v_rcp_f32_e32 v3, v3
	v_pk_add_f32 v[6:7], v[6:7], 2.0 op_sel_hi:[1,0] neg_lo:[1,0] neg_hi:[1,0]
	v_pk_mul_f32 v[0:1], v[0:1], v[4:5]
	v_pk_mul_f32 v[2:3], v[2:3], v[6:7]
	v_cvt_pk_fp8_f32 v8, v0, v1
	v_or_b32_e32 v4, 48, v200
	v_ashrrev_i32_e32 v5, 31, v4
	v_lshlrev_b64 v[4:5], 10, v[4:5]
	v_cvt_pk_fp8_f32 v8, v2, v3 op_sel:[0,0,1]
	v_lshl_add_u64 v[6:7], v[122:123], 0, v[4:5]
	global_store_dword v[6:7], v8, off sc1
	s_branch .LBB2_24
.Lmy_epi_l7:
	v_exp_f32_e32 v120, v120
	v_exp_f32_e32 v121, v121
	v_exp_f32_e32 v122, v122
	v_pk_add_f32 v[120:121], v[120:121], 1.0 op_sel_hi:[1,0]
	v_exp_f32_e32 v123, v123
	v_exp_f32_e32 v124, v124
	v_pk_add_f32 v[122:123], v[122:123], 1.0 op_sel_hi:[1,0]
	v_exp_f32_e32 v125, v125
	v_exp_f32_e32 v126, v126
	v_pk_add_f32 v[124:125], v[124:125], 1.0 op_sel_hi:[1,0]
	v_exp_f32_e32 v127, v127
	v_exp_f32_e32 v116, v116
	v_pk_add_f32 v[126:127], v[126:127], 1.0 op_sel_hi:[1,0]
	v_exp_f32_e32 v117, v117
	v_pk_mul_f32 v[120:121], v[120:121], v[124:125]
	v_exp_f32_e32 v118, v118
	v_pk_mul_f32 v[122:123], v[122:123], v[126:127]
	v_exp_f32_e32 v119, v119
	v_pk_add_f32 v[124:125], v[124:125], 2.0 op_sel_hi:[1,0] neg_lo:[1,0] neg_hi:[1,0]
	v_pk_add_f32 v[116:117], v[116:117], 1.0 op_sel_hi:[1,0]
	v_pk_add_f32 v[126:127], v[126:127], 2.0 op_sel_hi:[1,0] neg_lo:[1,0] neg_hi:[1,0]
	v_pk_add_f32 v[118:119], v[118:119], 1.0 op_sel_hi:[1,0]
	v_pk_mul_f32 v[124:125], v[124:125], v[116:117]
	v_pk_mul_f32 v[116:117], v[116:117], v[120:121]
	v_pk_mul_f32 v[126:127], v[126:127], v[118:119]
	v_pk_mul_f32 v[118:119], v[118:119], v[122:123]
	v_rcp_f32_e32 v116, v116
	v_rcp_f32_e32 v117, v117
	v_rcp_f32_e32 v118, v118
	v_rcp_f32_e32 v119, v119
	s_waitcnt lgkmcnt(3)
	v_pk_fma_f32 v[124:125], v[172:173], v[120:121], v[124:125]
	v_pk_fma_f32 v[126:127], v[174:175], v[122:123], v[126:127]
	v_pk_mul_f32 v[116:117], v[116:117], v[124:125]
	v_pk_mul_f32 v[118:119], v[118:119], v[126:127]
	global_store_dwordx4 v[176:177], v[116:119], off sc1
	s_nop 1
	v_pk_mul_f32 v[116:117], v[116:117], s[96:97] op_sel_hi:[1,0]
	v_pk_mul_f32 v[118:119], v[118:119], s[96:97] op_sel_hi:[1,0]
	v_exp_f32_e32 v112, v112
	v_exp_f32_e32 v113, v113
	v_exp_f32_e32 v114, v114
	v_pk_fma_f32 v[112:113], v[112:113], s[98:99], s[98:99] op_sel_hi:[1,0,0]
	v_exp_f32_e32 v115, v115
	v_exp_f32_e32 v116, v116
	v_pk_fma_f32 v[114:115], v[114:115], s[98:99], s[98:99] op_sel_hi:[1,0,0]
	v_exp_f32_e32 v117, v117
	v_exp_f32_e32 v118, v118
	v_pk_add_f32 v[116:117], v[116:117], 1.0 op_sel_hi:[1,0]
	v_exp_f32_e32 v119, v119
	v_pk_mul_f32 v[112:113], v[112:113], v[116:117]
	v_rcp_f32_e32 v112, v112
	v_pk_add_f32 v[118:119], v[118:119], 1.0 op_sel_hi:[1,0]
	v_rcp_f32_e32 v113, v113
	v_pk_mul_f32 v[114:115], v[114:115], v[118:119]
	v_pk_add_f32 v[116:117], v[116:117], 2.0 op_sel_hi:[1,0] neg_lo:[1,0] neg_hi:[1,0]
	v_rcp_f32_e32 v114, v114
	v_rcp_f32_e32 v115, v115
	v_pk_add_f32 v[118:119], v[118:119], 2.0 op_sel_hi:[1,0] neg_lo:[1,0] neg_hi:[1,0]
	v_pk_mul_f32 v[112:113], v[112:113], v[116:117]
	v_pk_mul_f32 v[114:115], v[114:115], v[118:119]
	v_cvt_pk_fp8_f32 v124, v112, v113
	s_add_u32 s0, s8, s27
	s_addc_u32 s1, s9, 0
	s_ashr_i32 s35, s34, 31
	s_lshl_b64 s[34:35], s[34:35], 21
	v_ashrrev_i32_e32 v209, 31, v208
	s_add_u32 s36, s73, s34
	v_lshrrev_b32_e32 v126, 4, v210
	v_and_b32_e32 v127, 15, v210
	v_lshl_or_b32 v126, v126, 8, v127
	v_and_b32_e32 v127, 15, v208
	v_mul_u32_u24_e32 v127, 0x3f0, v127
	v_sub_u32_e32 v126, v126, v127
	v_ashrrev_i32_e32 v127, 31, v126
	v_lshl_add_u64 v[122:123], s[0:1], 0, v[126:127]
	v_cvt_pk_fp8_f32 v124, v114, v115 op_sel:[0,0,1]
	v_lshlrev_b64 v[116:117], 10, v[208:209]
	s_addc_u32 s37, s74, s35
	v_lshl_add_u64 v[118:119], v[122:123], 0, v[116:117]
	global_store_dword v[118:119], v124, off sc1
	s_cmp_eq_u32 s30, 7
	s_cselect_b64 s[34:35], -1, 0
	s_cmp_lg_u32 s30, 7
	v_lshrrev_b32_e32 v126, 4, v210
	v_lshlrev_b32_e32 v126, 9, v126
	v_and_b32_e32 v127, 15, v210
	v_lshl_or_b32 v126, v127, 1, v126
	v_and_b32_e32 v127, 15, v208
	v_mul_u32_u24_e32 v127, 0x7e0, v127
	v_sub_u32_e32 v126, v126, v127
	v_ashrrev_i32_e32 v127, 31, v126
	v_lshl_add_u64 v[120:121], s[36:37], 0, v[126:127]
	v_pk_mul_f32 v[112:113], v[112:113], s[98:99] op_sel_hi:[1,0]
	v_pk_mul_f32 v[114:115], v[114:115], s[98:99] op_sel_hi:[1,0]
	v_cvt_pk_f16_f32 v112, v112, v113
	v_cvt_pk_f16_f32 v113, v114, v115
	v_lshl_add_u64 v[114:115], v[116:117], 1, v[120:121]
	global_store_dwordx2 v[114:115], v[112:113], off sc1
	v_exp_f32_e32 v104, v104
	v_exp_f32_e32 v105, v105
	v_exp_f32_e32 v106, v106
	v_pk_add_f32 v[104:105], v[104:105], 1.0 op_sel_hi:[1,0]
	v_exp_f32_e32 v107, v107
	v_exp_f32_e32 v108, v108
	v_pk_add_f32 v[106:107], v[106:107], 1.0 op_sel_hi:[1,0]
	v_exp_f32_e32 v109, v109
	v_exp_f32_e32 v110, v110
	v_pk_add_f32 v[108:109], v[108:109], 1.0 op_sel_hi:[1,0]
	v_exp_f32_e32 v111, v111
	v_exp_f32_e32 v100, v100
	v_pk_add_f32 v[110:111], v[110:111], 1.0 op_sel_hi:[1,0]
	v_exp_f32_e32 v101, v101
	v_pk_mul_f32 v[104:105], v[104:105], v[108:109]
	v_exp_f32_e32 v102, v102
	v_pk_mul_f32 v[106:107], v[106:107], v[110:111]
	v_exp_f32_e32 v103, v103
	v_pk_add_f32 v[108:109], v[108:109], 2.0 op_sel_hi:[1,0] neg_lo:[1,0] neg_hi:[1,0]
	v_pk_add_f32 v[100:101], v[100:101], 1.0 op_sel_hi:[1,0]
	v_pk_add_f32 v[110:111], v[110:111], 2.0 op_sel_hi:[1,0] neg_lo:[1,0] neg_hi:[1,0]
	v_pk_add_f32 v[102:103], v[102:103], 1.0 op_sel_hi:[1,0]
	v_pk_mul_f32 v[108:109], v[108:109], v[100:101]
	v_pk_mul_f32 v[100:101], v[100:101], v[104:105]
	v_pk_mul_f32 v[110:111], v[110:111], v[102:103]
	v_pk_mul_f32 v[102:103], v[102:103], v[106:107]
	v_rcp_f32_e32 v100, v100
	v_rcp_f32_e32 v101, v101
	v_rcp_f32_e32 v102, v102
	v_rcp_f32_e32 v103, v103
	s_waitcnt lgkmcnt(2)
	v_pk_fma_f32 v[108:109], v[168:169], v[104:105], v[108:109]
	v_pk_fma_f32 v[110:111], v[170:171], v[106:107], v[110:111]
	v_lshl_add_u64 v[104:105], v[176:177], 0, s[18:19]
	v_pk_mul_f32 v[100:101], v[100:101], v[108:109]
	v_pk_mul_f32 v[102:103], v[102:103], v[110:111]
	global_store_dwordx4 v[104:105], v[100:103], off sc1
	s_nop 1
	v_pk_mul_f32 v[100:101], v[100:101], s[96:97] op_sel_hi:[1,0]
	v_pk_mul_f32 v[102:103], v[102:103], s[96:97] op_sel_hi:[1,0]
	v_exp_f32_e32 v96, v96
	v_exp_f32_e32 v97, v97
	v_exp_f32_e32 v98, v98
	v_pk_fma_f32 v[96:97], v[96:97], s[98:99], s[98:99] op_sel_hi:[1,0,0]
	v_exp_f32_e32 v99, v99
	v_exp_f32_e32 v100, v100
	v_pk_fma_f32 v[98:99], v[98:99], s[98:99], s[98:99] op_sel_hi:[1,0,0]
	v_exp_f32_e32 v101, v101
	v_exp_f32_e32 v102, v102
	v_pk_add_f32 v[100:101], v[100:101], 1.0 op_sel_hi:[1,0]
	v_exp_f32_e32 v103, v103
	v_pk_mul_f32 v[96:97], v[96:97], v[100:101]
	v_rcp_f32_e32 v96, v96
	v_pk_add_f32 v[102:103], v[102:103], 1.0 op_sel_hi:[1,0]
	v_rcp_f32_e32 v97, v97
	v_pk_mul_f32 v[98:99], v[98:99], v[102:103]
	v_pk_add_f32 v[100:101], v[100:101], 2.0 op_sel_hi:[1,0] neg_lo:[1,0] neg_hi:[1,0]
	v_rcp_f32_e32 v98, v98
	v_rcp_f32_e32 v99, v99
	v_pk_add_f32 v[102:103], v[102:103], 2.0 op_sel_hi:[1,0] neg_lo:[1,0] neg_hi:[1,0]
	v_pk_mul_f32 v[96:97], v[96:97], v[100:101]
	v_pk_mul_f32 v[98:99], v[98:99], v[102:103]
	v_cvt_pk_fp8_f32 v104, v96, v97
	v_ashrrev_i32_e32 v207, 31, v206
	v_lshlrev_b64 v[100:101], 10, v[206:207]
	v_lshl_add_u64 v[102:103], v[122:123], 0, v[100:101]
	v_cvt_pk_fp8_f32 v104, v98, v99 op_sel:[0,0,1]
	v_cndmask_b32_e64 v105, 0, 1, s[34:35]
	global_store_dword v[102:103], v104, off sc1
	v_cmp_ne_u32_e64 s[0:1], 1, v105
	v_pk_mul_f32 v[96:97], v[96:97], s[98:99] op_sel_hi:[1,0]
	v_pk_mul_f32 v[98:99], v[98:99], s[98:99] op_sel_hi:[1,0]
	v_cvt_pk_f16_f32 v96, v96, v97
	v_cvt_pk_f16_f32 v97, v98, v99
	v_lshl_add_u64 v[98:99], v[100:101], 1, v[120:121]
	global_store_dwordx2 v[98:99], v[96:97], off sc1
	v_exp_f32_e32 v88, v88
	v_exp_f32_e32 v89, v89
	v_exp_f32_e32 v90, v90
	v_pk_add_f32 v[88:89], v[88:89], 1.0 op_sel_hi:[1,0]
	v_exp_f32_e32 v91, v91
	v_exp_f32_e32 v92, v92
	v_pk_add_f32 v[90:91], v[90:91], 1.0 op_sel_hi:[1,0]
	v_exp_f32_e32 v93, v93
	v_exp_f32_e32 v94, v94
	v_pk_add_f32 v[92:93], v[92:93], 1.0 op_sel_hi:[1,0]
	v_exp_f32_e32 v95, v95
	v_exp_f32_e32 v84, v84
	v_pk_add_f32 v[94:95], v[94:95], 1.0 op_sel_hi:[1,0]
	v_exp_f32_e32 v85, v85
	v_pk_mul_f32 v[88:89], v[88:89], v[92:93]
	v_exp_f32_e32 v86, v86
	v_pk_mul_f32 v[90:91], v[90:91], v[94:95]
	v_exp_f32_e32 v87, v87
	v_pk_add_f32 v[92:93], v[92:93], 2.0 op_sel_hi:[1,0] neg_lo:[1,0] neg_hi:[1,0]
	v_pk_add_f32 v[84:85], v[84:85], 1.0 op_sel_hi:[1,0]
	v_pk_add_f32 v[94:95], v[94:95], 2.0 op_sel_hi:[1,0] neg_lo:[1,0] neg_hi:[1,0]
	v_pk_add_f32 v[86:87], v[86:87], 1.0 op_sel_hi:[1,0]
	v_pk_mul_f32 v[92:93], v[92:93], v[84:85]
	v_pk_mul_f32 v[84:85], v[84:85], v[88:89]
	v_pk_mul_f32 v[94:95], v[94:95], v[86:87]
	v_pk_mul_f32 v[86:87], v[86:87], v[90:91]
	v_rcp_f32_e32 v84, v84
	v_rcp_f32_e32 v85, v85
	v_rcp_f32_e32 v86, v86
	v_rcp_f32_e32 v87, v87
	s_waitcnt lgkmcnt(1)
	v_pk_fma_f32 v[92:93], v[164:165], v[88:89], v[92:93]
	v_pk_fma_f32 v[94:95], v[166:167], v[90:91], v[94:95]
	v_pk_mul_f32 v[84:85], v[84:85], v[92:93]
	v_pk_mul_f32 v[86:87], v[86:87], v[94:95]
	v_lshl_add_u64 v[88:89], v[176:177], 0, s[12:13]
	global_store_dwordx4 v[88:89], v[84:87], off sc1
	s_nop 1
	v_pk_mul_f32 v[84:85], v[84:85], s[96:97] op_sel_hi:[1,0]
	v_pk_mul_f32 v[86:87], v[86:87], s[96:97] op_sel_hi:[1,0]
	v_exp_f32_e32 v80, v80
	v_exp_f32_e32 v81, v81
	v_exp_f32_e32 v82, v82
	v_pk_fma_f32 v[80:81], v[80:81], s[98:99], s[98:99] op_sel_hi:[1,0,0]
	v_exp_f32_e32 v83, v83
	v_exp_f32_e32 v84, v84
	v_pk_fma_f32 v[82:83], v[82:83], s[98:99], s[98:99] op_sel_hi:[1,0,0]
	v_exp_f32_e32 v85, v85
	v_exp_f32_e32 v86, v86
	v_pk_add_f32 v[84:85], v[84:85], 1.0 op_sel_hi:[1,0]
	v_exp_f32_e32 v87, v87
	v_pk_mul_f32 v[80:81], v[80:81], v[84:85]
	v_rcp_f32_e32 v80, v80
	v_pk_add_f32 v[86:87], v[86:87], 1.0 op_sel_hi:[1,0]
	v_rcp_f32_e32 v81, v81
	v_pk_mul_f32 v[82:83], v[82:83], v[86:87]
	v_pk_add_f32 v[84:85], v[84:85], 2.0 op_sel_hi:[1,0] neg_lo:[1,0] neg_hi:[1,0]
	v_rcp_f32_e32 v82, v82
	v_rcp_f32_e32 v83, v83
	v_pk_add_f32 v[86:87], v[86:87], 2.0 op_sel_hi:[1,0] neg_lo:[1,0] neg_hi:[1,0]
	v_pk_mul_f32 v[80:81], v[80:81], v[84:85]
	v_pk_mul_f32 v[82:83], v[82:83], v[86:87]
	v_ashrrev_i32_e32 v205, 31, v204
	v_cvt_pk_fp8_f32 v88, v80, v81
	s_and_b64 vcc, exec, s[0:1]
	v_cvt_pk_fp8_f32 v88, v82, v83 op_sel:[0,0,1]
	v_lshlrev_b64 v[84:85], 10, v[204:205]
	v_lshl_add_u64 v[86:87], v[122:123], 0, v[84:85]
	global_store_dword v[86:87], v88, off sc1
	v_pk_mul_f32 v[80:81], v[80:81], s[98:99] op_sel_hi:[1,0]
	v_pk_mul_f32 v[82:83], v[82:83], s[98:99] op_sel_hi:[1,0]
	v_cvt_pk_f16_f32 v80, v80, v81
	v_cvt_pk_f16_f32 v81, v82, v83
	v_lshl_add_u64 v[82:83], v[84:85], 1, v[120:121]
	global_store_dwordx2 v[82:83], v[80:81], off sc1
	v_exp_f32_e32 v72, v72
	v_exp_f32_e32 v73, v73
	v_exp_f32_e32 v74, v74
	v_pk_add_f32 v[72:73], v[72:73], 1.0 op_sel_hi:[1,0]
	v_exp_f32_e32 v75, v75
	v_exp_f32_e32 v76, v76
	v_pk_add_f32 v[74:75], v[74:75], 1.0 op_sel_hi:[1,0]
	v_exp_f32_e32 v77, v77
	v_exp_f32_e32 v78, v78
	v_pk_add_f32 v[76:77], v[76:77], 1.0 op_sel_hi:[1,0]
	v_exp_f32_e32 v79, v79
	v_exp_f32_e32 v68, v68
	v_pk_add_f32 v[78:79], v[78:79], 1.0 op_sel_hi:[1,0]
	v_exp_f32_e32 v69, v69
	v_pk_mul_f32 v[72:73], v[72:73], v[76:77]
	v_exp_f32_e32 v70, v70
	v_pk_mul_f32 v[74:75], v[74:75], v[78:79]
	v_exp_f32_e32 v71, v71
	v_pk_add_f32 v[76:77], v[76:77], 2.0 op_sel_hi:[1,0] neg_lo:[1,0] neg_hi:[1,0]
	v_pk_add_f32 v[68:69], v[68:69], 1.0 op_sel_hi:[1,0]
	v_pk_add_f32 v[78:79], v[78:79], 2.0 op_sel_hi:[1,0] neg_lo:[1,0] neg_hi:[1,0]
	v_pk_add_f32 v[70:71], v[70:71], 1.0 op_sel_hi:[1,0]
	v_pk_mul_f32 v[76:77], v[76:77], v[68:69]
	v_pk_mul_f32 v[68:69], v[68:69], v[72:73]
	v_pk_mul_f32 v[78:79], v[78:79], v[70:71]
	v_pk_mul_f32 v[70:71], v[70:71], v[74:75]
	v_rcp_f32_e32 v68, v68
	v_rcp_f32_e32 v69, v69
	v_rcp_f32_e32 v70, v70
	v_rcp_f32_e32 v71, v71
	s_waitcnt lgkmcnt(0)
	v_pk_fma_f32 v[76:77], v[160:161], v[72:73], v[76:77]
	v_pk_fma_f32 v[78:79], v[162:163], v[74:75], v[78:79]
	v_lshl_add_u64 v[72:73], v[176:177], 0, s[20:21]
	v_pk_mul_f32 v[68:69], v[68:69], v[76:77]
	v_pk_mul_f32 v[70:71], v[70:71], v[78:79]
	global_store_dwordx4 v[72:73], v[68:71], off sc1
	s_nop 1
	v_pk_mul_f32 v[68:69], v[68:69], s[96:97] op_sel_hi:[1,0]
	v_pk_mul_f32 v[70:71], v[70:71], s[96:97] op_sel_hi:[1,0]
	v_exp_f32_e32 v64, v64
	v_exp_f32_e32 v65, v65
	v_exp_f32_e32 v66, v66
	v_pk_fma_f32 v[64:65], v[64:65], s[98:99], s[98:99] op_sel_hi:[1,0,0]
	v_exp_f32_e32 v67, v67
	v_exp_f32_e32 v68, v68
	v_pk_fma_f32 v[66:67], v[66:67], s[98:99], s[98:99] op_sel_hi:[1,0,0]
	v_exp_f32_e32 v69, v69
	v_exp_f32_e32 v70, v70
	v_pk_add_f32 v[68:69], v[68:69], 1.0 op_sel_hi:[1,0]
	v_exp_f32_e32 v71, v71
	v_pk_mul_f32 v[64:65], v[64:65], v[68:69]
	v_rcp_f32_e32 v64, v64
	v_pk_add_f32 v[70:71], v[70:71], 1.0 op_sel_hi:[1,0]
	v_rcp_f32_e32 v65, v65
	v_pk_mul_f32 v[66:67], v[66:67], v[70:71]
	v_pk_add_f32 v[68:69], v[68:69], 2.0 op_sel_hi:[1,0] neg_lo:[1,0] neg_hi:[1,0]
	v_rcp_f32_e32 v66, v66
	v_rcp_f32_e32 v67, v67
	v_pk_add_f32 v[70:71], v[70:71], 2.0 op_sel_hi:[1,0] neg_lo:[1,0] neg_hi:[1,0]
	v_pk_mul_f32 v[64:65], v[64:65], v[68:69]
	v_pk_mul_f32 v[66:67], v[66:67], v[70:71]
	v_ashrrev_i32_e32 v203, 31, v202
	v_cvt_pk_fp8_f32 v72, v64, v65
	s_and_b64 vcc, exec, s[0:1]
	v_cvt_pk_fp8_f32 v72, v66, v67 op_sel:[0,0,1]
	v_lshlrev_b64 v[68:69], 10, v[202:203]
	v_lshl_add_u64 v[70:71], v[122:123], 0, v[68:69]
	global_store_dword v[70:71], v72, off sc1
	v_pk_mul_f32 v[64:65], v[64:65], s[98:99] op_sel_hi:[1,0]
	v_pk_mul_f32 v[66:67], v[66:67], s[98:99] op_sel_hi:[1,0]
	v_cvt_pk_f16_f32 v64, v64, v65
	v_cvt_pk_f16_f32 v65, v66, v67
	v_lshl_add_u64 v[66:67], v[68:69], 1, v[120:121]
	global_store_dwordx2 v[66:67], v[64:65], off sc1
	v_exp_f32_e32 v56, v56
	v_exp_f32_e32 v57, v57
	v_exp_f32_e32 v58, v58
	v_pk_add_f32 v[56:57], v[56:57], 1.0 op_sel_hi:[1,0]
	v_exp_f32_e32 v59, v59
	v_exp_f32_e32 v60, v60
	v_pk_add_f32 v[58:59], v[58:59], 1.0 op_sel_hi:[1,0]
	v_exp_f32_e32 v61, v61
	v_exp_f32_e32 v62, v62
	v_pk_add_f32 v[60:61], v[60:61], 1.0 op_sel_hi:[1,0]
	v_exp_f32_e32 v63, v63
	v_exp_f32_e32 v52, v52
	v_pk_add_f32 v[62:63], v[62:63], 1.0 op_sel_hi:[1,0]
	v_exp_f32_e32 v53, v53
	v_pk_mul_f32 v[56:57], v[56:57], v[60:61]
	v_exp_f32_e32 v54, v54
	v_pk_mul_f32 v[58:59], v[58:59], v[62:63]
	v_exp_f32_e32 v55, v55
	v_pk_add_f32 v[60:61], v[60:61], 2.0 op_sel_hi:[1,0] neg_lo:[1,0] neg_hi:[1,0]
	v_pk_add_f32 v[52:53], v[52:53], 1.0 op_sel_hi:[1,0]
	v_pk_add_f32 v[62:63], v[62:63], 2.0 op_sel_hi:[1,0] neg_lo:[1,0] neg_hi:[1,0]
	v_pk_add_f32 v[54:55], v[54:55], 1.0 op_sel_hi:[1,0]
	v_pk_mul_f32 v[60:61], v[60:61], v[52:53]
	v_pk_mul_f32 v[52:53], v[52:53], v[56:57]
	v_pk_mul_f32 v[62:63], v[62:63], v[54:55]
	v_pk_mul_f32 v[54:55], v[54:55], v[58:59]
	v_rcp_f32_e32 v52, v52
	v_rcp_f32_e32 v53, v53
	v_rcp_f32_e32 v54, v54
	v_rcp_f32_e32 v55, v55
	s_waitcnt vmcnt(8)
	v_pk_fma_f32 v[60:61], v[156:157], v[56:57], v[60:61]
	v_pk_fma_f32 v[62:63], v[158:159], v[58:59], v[62:63]
	v_pk_mul_f32 v[52:53], v[52:53], v[60:61]
	v_pk_mul_f32 v[54:55], v[54:55], v[62:63]
	v_lshl_add_u64 v[56:57], v[176:177], 0, s[14:15]
	global_store_dwordx4 v[56:57], v[52:55], off sc1
	s_nop 1
	v_pk_mul_f32 v[52:53], v[52:53], s[96:97] op_sel_hi:[1,0]
	v_pk_mul_f32 v[54:55], v[54:55], s[96:97] op_sel_hi:[1,0]
	v_exp_f32_e32 v48, v48
	v_exp_f32_e32 v49, v49
	v_exp_f32_e32 v50, v50
	v_pk_fma_f32 v[48:49], v[48:49], s[98:99], s[98:99] op_sel_hi:[1,0,0]
	v_exp_f32_e32 v51, v51
	v_exp_f32_e32 v52, v52
	v_pk_fma_f32 v[50:51], v[50:51], s[98:99], s[98:99] op_sel_hi:[1,0,0]
	v_exp_f32_e32 v53, v53
	v_exp_f32_e32 v54, v54
	v_pk_add_f32 v[52:53], v[52:53], 1.0 op_sel_hi:[1,0]
	v_exp_f32_e32 v55, v55
	v_pk_mul_f32 v[48:49], v[48:49], v[52:53]
	v_rcp_f32_e32 v48, v48
	v_pk_add_f32 v[54:55], v[54:55], 1.0 op_sel_hi:[1,0]
	v_rcp_f32_e32 v49, v49
	v_pk_mul_f32 v[50:51], v[50:51], v[54:55]
	v_pk_add_f32 v[52:53], v[52:53], 2.0 op_sel_hi:[1,0] neg_lo:[1,0] neg_hi:[1,0]
	v_rcp_f32_e32 v50, v50
	v_rcp_f32_e32 v51, v51
	v_pk_add_f32 v[54:55], v[54:55], 2.0 op_sel_hi:[1,0] neg_lo:[1,0] neg_hi:[1,0]
	v_pk_mul_f32 v[48:49], v[48:49], v[52:53]
	v_pk_mul_f32 v[50:51], v[50:51], v[54:55]
	v_ashrrev_i32_e32 v201, 31, v200
	v_cvt_pk_fp8_f32 v56, v48, v49
	s_and_b64 vcc, exec, s[0:1]
	v_cvt_pk_fp8_f32 v56, v50, v51 op_sel:[0,0,1]
	v_lshlrev_b64 v[52:53], 10, v[200:201]
	v_lshl_add_u64 v[54:55], v[122:123], 0, v[52:53]
	global_store_dword v[54:55], v56, off sc1
	v_pk_mul_f32 v[48:49], v[48:49], s[98:99] op_sel_hi:[1,0]
	v_pk_mul_f32 v[50:51], v[50:51], s[98:99] op_sel_hi:[1,0]
	v_cvt_pk_f16_f32 v48, v48, v49
	v_cvt_pk_f16_f32 v49, v50, v51
	v_lshl_add_u64 v[50:51], v[52:53], 1, v[120:121]
	global_store_dwordx2 v[50:51], v[48:49], off sc1
	v_exp_f32_e32 v40, v40
	v_exp_f32_e32 v41, v41
	v_exp_f32_e32 v42, v42
	v_pk_add_f32 v[40:41], v[40:41], 1.0 op_sel_hi:[1,0]
	v_exp_f32_e32 v43, v43
	v_exp_f32_e32 v44, v44
	v_pk_add_f32 v[42:43], v[42:43], 1.0 op_sel_hi:[1,0]
	v_exp_f32_e32 v45, v45
	v_exp_f32_e32 v46, v46
	v_pk_add_f32 v[44:45], v[44:45], 1.0 op_sel_hi:[1,0]
	v_exp_f32_e32 v47, v47
	v_exp_f32_e32 v36, v36
	v_pk_add_f32 v[46:47], v[46:47], 1.0 op_sel_hi:[1,0]
	v_exp_f32_e32 v37, v37
	v_pk_mul_f32 v[40:41], v[40:41], v[44:45]
	v_exp_f32_e32 v38, v38
	v_pk_mul_f32 v[42:43], v[42:43], v[46:47]
	v_exp_f32_e32 v39, v39
	v_pk_add_f32 v[44:45], v[44:45], 2.0 op_sel_hi:[1,0] neg_lo:[1,0] neg_hi:[1,0]
	v_pk_add_f32 v[36:37], v[36:37], 1.0 op_sel_hi:[1,0]
	v_pk_add_f32 v[46:47], v[46:47], 2.0 op_sel_hi:[1,0] neg_lo:[1,0] neg_hi:[1,0]
	v_pk_add_f32 v[38:39], v[38:39], 1.0 op_sel_hi:[1,0]
	v_pk_mul_f32 v[44:45], v[44:45], v[36:37]
	v_pk_mul_f32 v[36:37], v[36:37], v[40:41]
	v_pk_mul_f32 v[46:47], v[46:47], v[38:39]
	v_pk_mul_f32 v[38:39], v[38:39], v[42:43]
	v_rcp_f32_e32 v36, v36
	v_rcp_f32_e32 v37, v37
	v_rcp_f32_e32 v38, v38
	v_rcp_f32_e32 v39, v39
	v_pk_fma_f32 v[44:45], v[152:153], v[40:41], v[44:45]
	v_pk_fma_f32 v[46:47], v[154:155], v[42:43], v[46:47]
	v_lshl_add_u64 v[40:41], v[176:177], 0, s[22:23]
	v_pk_mul_f32 v[36:37], v[36:37], v[44:45]
	v_pk_mul_f32 v[38:39], v[38:39], v[46:47]
	global_store_dwordx4 v[40:41], v[36:39], off sc1
	s_nop 1
	v_pk_mul_f32 v[36:37], v[36:37], s[96:97] op_sel_hi:[1,0]
	v_pk_mul_f32 v[38:39], v[38:39], s[96:97] op_sel_hi:[1,0]
	v_exp_f32_e32 v32, v32
	v_exp_f32_e32 v33, v33
	v_exp_f32_e32 v34, v34
	v_pk_fma_f32 v[32:33], v[32:33], s[98:99], s[98:99] op_sel_hi:[1,0,0]
	v_exp_f32_e32 v35, v35
	v_exp_f32_e32 v36, v36
	v_pk_fma_f32 v[34:35], v[34:35], s[98:99], s[98:99] op_sel_hi:[1,0,0]
	v_exp_f32_e32 v37, v37
	v_exp_f32_e32 v38, v38
	v_pk_add_f32 v[36:37], v[36:37], 1.0 op_sel_hi:[1,0]
	v_exp_f32_e32 v39, v39
	v_pk_mul_f32 v[32:33], v[32:33], v[36:37]
	v_rcp_f32_e32 v32, v32
	v_pk_add_f32 v[38:39], v[38:39], 1.0 op_sel_hi:[1,0]
	v_rcp_f32_e32 v33, v33
	v_pk_mul_f32 v[34:35], v[34:35], v[38:39]
	v_pk_add_f32 v[36:37], v[36:37], 2.0 op_sel_hi:[1,0] neg_lo:[1,0] neg_hi:[1,0]
	v_rcp_f32_e32 v34, v34
	v_rcp_f32_e32 v35, v35
	v_pk_add_f32 v[38:39], v[38:39], 2.0 op_sel_hi:[1,0] neg_lo:[1,0] neg_hi:[1,0]
	v_pk_mul_f32 v[32:33], v[32:33], v[36:37]
	v_pk_mul_f32 v[34:35], v[34:35], v[38:39]
	v_cvt_pk_fp8_f32 v40, v32, v33
	v_or_b32_e32 v36, 16, v200
	v_ashrrev_i32_e32 v37, 31, v36
	v_lshlrev_b64 v[36:37], 10, v[36:37]
	v_cvt_pk_fp8_f32 v40, v34, v35 op_sel:[0,0,1]
	v_lshl_add_u64 v[38:39], v[122:123], 0, v[36:37]
	global_store_dword v[38:39], v40, off sc1
	v_pk_mul_f32 v[32:33], v[32:33], s[98:99] op_sel_hi:[1,0]
	v_pk_mul_f32 v[34:35], v[34:35], s[98:99] op_sel_hi:[1,0]
	v_cvt_pk_f16_f32 v32, v32, v33
	v_cvt_pk_f16_f32 v33, v34, v35
	v_lshl_add_u64 v[34:35], v[36:37], 1, v[120:121]
	global_store_dwordx2 v[34:35], v[32:33], off sc1
	v_exp_f32_e32 v24, v24
	v_exp_f32_e32 v25, v25
	v_exp_f32_e32 v26, v26
	v_pk_add_f32 v[24:25], v[24:25], 1.0 op_sel_hi:[1,0]
	v_exp_f32_e32 v27, v27
	v_exp_f32_e32 v28, v28
	v_pk_add_f32 v[26:27], v[26:27], 1.0 op_sel_hi:[1,0]
	v_exp_f32_e32 v29, v29
	v_exp_f32_e32 v30, v30
	v_pk_add_f32 v[28:29], v[28:29], 1.0 op_sel_hi:[1,0]
	v_exp_f32_e32 v31, v31
	v_exp_f32_e32 v20, v20
	v_pk_add_f32 v[30:31], v[30:31], 1.0 op_sel_hi:[1,0]
	v_exp_f32_e32 v21, v21
	v_pk_mul_f32 v[24:25], v[24:25], v[28:29]
	v_exp_f32_e32 v22, v22
	v_pk_mul_f32 v[26:27], v[26:27], v[30:31]
	v_exp_f32_e32 v23, v23
	v_pk_add_f32 v[28:29], v[28:29], 2.0 op_sel_hi:[1,0] neg_lo:[1,0] neg_hi:[1,0]
	v_pk_add_f32 v[20:21], v[20:21], 1.0 op_sel_hi:[1,0]
	v_pk_add_f32 v[30:31], v[30:31], 2.0 op_sel_hi:[1,0] neg_lo:[1,0] neg_hi:[1,0]
	v_pk_add_f32 v[22:23], v[22:23], 1.0 op_sel_hi:[1,0]
	v_pk_mul_f32 v[28:29], v[28:29], v[20:21]
	v_pk_mul_f32 v[20:21], v[20:21], v[24:25]
	v_pk_mul_f32 v[30:31], v[30:31], v[22:23]
	v_pk_mul_f32 v[22:23], v[22:23], v[26:27]
	v_rcp_f32_e32 v20, v20
	v_rcp_f32_e32 v21, v21
	v_rcp_f32_e32 v22, v22
	v_rcp_f32_e32 v23, v23
	v_pk_fma_f32 v[28:29], v[148:149], v[24:25], v[28:29]
	v_pk_fma_f32 v[30:31], v[150:151], v[26:27], v[30:31]
	v_pk_mul_f32 v[20:21], v[20:21], v[28:29]
	v_pk_mul_f32 v[22:23], v[22:23], v[30:31]
	v_lshl_add_u64 v[24:25], v[176:177], 0, s[16:17]
	global_store_dwordx4 v[24:25], v[20:23], off sc1
	s_nop 1
	v_pk_mul_f32 v[20:21], v[20:21], s[96:97] op_sel_hi:[1,0]
	v_pk_mul_f32 v[22:23], v[22:23], s[96:97] op_sel_hi:[1,0]
	v_exp_f32_e32 v16, v16
	v_exp_f32_e32 v17, v17
	v_exp_f32_e32 v18, v18
	v_pk_fma_f32 v[16:17], v[16:17], s[98:99], s[98:99] op_sel_hi:[1,0,0]
	v_exp_f32_e32 v19, v19
	v_exp_f32_e32 v20, v20
	v_pk_fma_f32 v[18:19], v[18:19], s[98:99], s[98:99] op_sel_hi:[1,0,0]
	v_exp_f32_e32 v21, v21
	v_exp_f32_e32 v22, v22
	v_pk_add_f32 v[20:21], v[20:21], 1.0 op_sel_hi:[1,0]
	v_exp_f32_e32 v23, v23
	v_pk_mul_f32 v[16:17], v[16:17], v[20:21]
	v_rcp_f32_e32 v16, v16
	v_pk_add_f32 v[22:23], v[22:23], 1.0 op_sel_hi:[1,0]
	v_rcp_f32_e32 v17, v17
	v_pk_mul_f32 v[18:19], v[18:19], v[22:23]
	v_pk_add_f32 v[20:21], v[20:21], 2.0 op_sel_hi:[1,0] neg_lo:[1,0] neg_hi:[1,0]
	v_rcp_f32_e32 v18, v18
	v_rcp_f32_e32 v19, v19
	v_pk_add_f32 v[22:23], v[22:23], 2.0 op_sel_hi:[1,0] neg_lo:[1,0] neg_hi:[1,0]
	v_pk_mul_f32 v[16:17], v[16:17], v[20:21]
	v_pk_mul_f32 v[18:19], v[18:19], v[22:23]
	v_cvt_pk_fp8_f32 v24, v16, v17
	v_or_b32_e32 v20, 32, v200
	v_ashrrev_i32_e32 v21, 31, v20
	v_lshlrev_b64 v[20:21], 10, v[20:21]
	v_cvt_pk_fp8_f32 v24, v18, v19 op_sel:[0,0,1]
	v_lshl_add_u64 v[22:23], v[122:123], 0, v[20:21]
	global_store_dword v[22:23], v24, off sc1
	v_pk_mul_f32 v[16:17], v[16:17], s[98:99] op_sel_hi:[1,0]
	v_pk_mul_f32 v[18:19], v[18:19], s[98:99] op_sel_hi:[1,0]
	v_cvt_pk_f16_f32 v16, v16, v17
	v_cvt_pk_f16_f32 v17, v18, v19
	v_lshl_add_u64 v[18:19], v[20:21], 1, v[120:121]
	global_store_dwordx2 v[18:19], v[16:17], off sc1
	v_exp_f32_e32 v8, v8
	v_exp_f32_e32 v9, v9
	v_exp_f32_e32 v10, v10
	v_pk_add_f32 v[8:9], v[8:9], 1.0 op_sel_hi:[1,0]
	v_exp_f32_e32 v11, v11
	v_exp_f32_e32 v12, v12
	v_pk_add_f32 v[10:11], v[10:11], 1.0 op_sel_hi:[1,0]
	v_exp_f32_e32 v13, v13
	v_exp_f32_e32 v14, v14
	v_pk_add_f32 v[12:13], v[12:13], 1.0 op_sel_hi:[1,0]
	v_exp_f32_e32 v15, v15
	v_exp_f32_e32 v4, v4
	v_pk_add_f32 v[14:15], v[14:15], 1.0 op_sel_hi:[1,0]
	v_exp_f32_e32 v5, v5
	v_pk_mul_f32 v[8:9], v[8:9], v[12:13]
	v_exp_f32_e32 v6, v6
	v_pk_mul_f32 v[10:11], v[10:11], v[14:15]
	v_exp_f32_e32 v7, v7
	v_pk_add_f32 v[12:13], v[12:13], 2.0 op_sel_hi:[1,0] neg_lo:[1,0] neg_hi:[1,0]
	v_pk_add_f32 v[4:5], v[4:5], 1.0 op_sel_hi:[1,0]
	v_pk_add_f32 v[14:15], v[14:15], 2.0 op_sel_hi:[1,0] neg_lo:[1,0] neg_hi:[1,0]
	v_pk_add_f32 v[6:7], v[6:7], 1.0 op_sel_hi:[1,0]
	v_pk_mul_f32 v[12:13], v[12:13], v[4:5]
	v_pk_mul_f32 v[4:5], v[4:5], v[8:9]
	v_pk_mul_f32 v[14:15], v[14:15], v[6:7]
	v_pk_mul_f32 v[6:7], v[6:7], v[10:11]
	v_rcp_f32_e32 v4, v4
	v_rcp_f32_e32 v5, v5
	v_rcp_f32_e32 v6, v6
	v_rcp_f32_e32 v7, v7
	v_pk_fma_f32 v[12:13], v[144:145], v[8:9], v[12:13]
	v_pk_fma_f32 v[14:15], v[146:147], v[10:11], v[14:15]
	v_lshl_add_u64 v[8:9], v[176:177], 0, s[24:25]
	v_pk_mul_f32 v[4:5], v[4:5], v[12:13]
	v_pk_mul_f32 v[6:7], v[6:7], v[14:15]
	global_store_dwordx4 v[8:9], v[4:7], off sc1
	s_nop 1
	v_pk_mul_f32 v[4:5], v[4:5], s[96:97] op_sel_hi:[1,0]
	v_pk_mul_f32 v[6:7], v[6:7], s[96:97] op_sel_hi:[1,0]
	v_exp_f32_e32 v0, v0
	v_exp_f32_e32 v1, v1
	v_exp_f32_e32 v2, v2
	v_pk_fma_f32 v[0:1], v[0:1], s[98:99], s[98:99] op_sel_hi:[1,0,0]
	v_exp_f32_e32 v3, v3
	v_exp_f32_e32 v4, v4
	v_pk_fma_f32 v[2:3], v[2:3], s[98:99], s[98:99] op_sel_hi:[1,0,0]
	v_exp_f32_e32 v5, v5
	v_exp_f32_e32 v6, v6
	v_pk_add_f32 v[4:5], v[4:5], 1.0 op_sel_hi:[1,0]
	v_exp_f32_e32 v7, v7
	v_pk_mul_f32 v[0:1], v[0:1], v[4:5]
	v_rcp_f32_e32 v0, v0
	v_pk_add_f32 v[6:7], v[6:7], 1.0 op_sel_hi:[1,0]
	v_rcp_f32_e32 v1, v1
	v_pk_mul_f32 v[2:3], v[2:3], v[6:7]
	v_pk_add_f32 v[4:5], v[4:5], 2.0 op_sel_hi:[1,0] neg_lo:[1,0] neg_hi:[1,0]
	v_rcp_f32_e32 v2, v2
	v_rcp_f32_e32 v3, v3
	v_pk_add_f32 v[6:7], v[6:7], 2.0 op_sel_hi:[1,0] neg_lo:[1,0] neg_hi:[1,0]
	v_pk_mul_f32 v[0:1], v[0:1], v[4:5]
	v_pk_mul_f32 v[2:3], v[2:3], v[6:7]
	v_cvt_pk_fp8_f32 v8, v0, v1
	v_or_b32_e32 v4, 48, v200
	v_ashrrev_i32_e32 v5, 31, v4
	v_lshlrev_b64 v[4:5], 10, v[4:5]
	v_cvt_pk_fp8_f32 v8, v2, v3 op_sel:[0,0,1]
	v_lshl_add_u64 v[6:7], v[122:123], 0, v[4:5]
	global_store_dword v[6:7], v8, off sc1
	v_pk_mul_f32 v[0:1], v[0:1], s[98:99] op_sel_hi:[1,0]
	v_pk_mul_f32 v[2:3], v[2:3], s[98:99] op_sel_hi:[1,0]
	v_cvt_pk_f16_f32 v0, v0, v1
	v_cvt_pk_f16_f32 v1, v2, v3
	v_lshl_add_u64 v[2:3], v[4:5], 1, v[120:121]
	global_store_dwordx2 v[2:3], v[0:1], off sc1
	s_branch .LBB2_24
